# n34_outlds
# speedup vs baseline: 1.0151x; 1.0080x over previous
.LBB2_15:
	v_ashrrev_i32_e32 v163, 31, v162
	v_lshl_or_b32 v164, s30, 4, v132
	v_lshlrev_b64 v[130:131], 11, v[162:163]
	v_mov_b32_e32 v167, 0
	s_waitcnt lgkmcnt(0)
	s_mov_b64 s[50:51], s[0:1]
	v_lshl_add_u64 v[130:131], s[0:1], 0, v[130:131]
	v_lshlrev_b32_e32 v166, 4, v164
	v_lshl_add_u64 v[168:169], v[130:131], 0, v[166:167]
	global_load_dwordx2 v[170:171], v[168:169], off nt
	v_lshlrev_b32_e32 v142, 4, v140
	v_cmp_gt_u32_e64 s[2:3], 16, v140
	v_mov_b32_e32 v140, 0x10000
	v_lshlrev_b32_e32 v130, 8, v139
	v_lshlrev_b32_e32 v131, 4, v132
	v_lshlrev_b32_e32 v132, 3, v138
	v_lshl_or_b32 v177, v138, 14, v142
	v_lshl_or_b32 v139, v139, 11, v140
	v_lshlrev_b32_e32 v140, 10, v138
	v_xor_b32_e32 v138, 1, v138
	v_lshlrev_b32_e32 v141, 12, v1
	v_lshlrev_b32_e32 v138, 10, v138
	v_or3_b32 v179, v139, v138, v142
	v_add_u32_e32 v138, 0x1000, v141
	v_and_b32_e32 v180, 0x3000, v138
	v_add_u32_e32 v138, 0x1400, v141
	v_and_b32_e32 v181, 0x3400, v138
	v_add_u32_e32 v138, 0x1800, v141
	v_and_b32_e32 v182, 0x3800, v138
	v_add_u32_e32 v138, 0x1c00, v141
	v_and_b32_e32 v183, 0x3c00, v138
	s_movk_i32 s4, 0x2000
	v_mov_b32_e32 v138, 0x3000
	v_bitop3_b32 v184, v141, s4, v138 bitop3:0x6c
	v_add_u32_e32 v138, 0x2400, v141
	v_and_b32_e32 v185, 0x3400, v138
	v_add_u32_e32 v138, 0x2800, v141
	v_and_b32_e32 v186, 0x3800, v138
	v_add_u32_e32 v138, 0x2c00, v141
	v_and_b32_e32 v187, 0x3c00, v138
	v_add_u32_e32 v138, 0x3000, v141
	v_and_b32_e32 v188, 0x3000, v138
	v_add_u32_e32 v138, 0x3400, v141
	s_and_b32 s9, s7, 0xffff
	v_cmp_eq_u32_e32 vcc, s14, v133
	v_lshl_or_b32 v131, s16, 10, v131
	s_movk_i32 s0, 0x100
	v_lshlrev_b32_e32 v166, 12, v164
	v_and_b32_e32 v189, 0x3400, v138
	v_add_u32_e32 v138, 0x3800, v141
	s_cmp_lg_u64 vcc, exec
	v_lshl_add_u32 v131, s30, 15, v131
	v_cmp_gt_u32_e64 s[0:1], s0, v0
	v_lshl_add_u64 v[0:1], s[12:13], 0, v[166:167]
	v_and_b32_e32 v190, 0x3800, v138
	v_add_u32_e32 v138, 0x3c00, v141
	v_mov_b32_e32 v172, -1
	s_mov_b32 s11, 0x20000
	s_mov_b32 s10, 0x200400
	s_mov_b32 s8, s6
	s_cselect_b64 s[14:15], -1, 0
	v_or3_b32 v165, v131, v132, v130
	s_mov_b32 s17, 0
	v_cndmask_b32_e64 v133, 0, v137, s[0:1]
	v_cndmask_b32_e64 v132, 0, v136, s[0:1]
	v_cndmask_b32_e64 v131, 0, v135, s[0:1]
	v_cndmask_b32_e64 v130, 0, v134, s[0:1]
	v_cndmask_b32_e64 v137, v137, 0, s[0:1]
	v_cndmask_b32_e64 v136, v136, 0, s[0:1]
	v_cndmask_b32_e64 v135, v135, 0, s[0:1]
	v_cndmask_b32_e64 v134, v134, 0, s[0:1]
	v_or_b32_e32 v176, v141, v142
	v_lshl_add_u64 v[0:1], v[162:163], 2, v[0:1]
	v_or3_b32 v178, v139, v140, v142
	v_and_b32_e32 v191, 0x3c00, v138
	s_mov_b64 s[24:25], 0
	s_mov_b64 s[18:19], 0x400
	s_mov_b64 s[20:21], 0x800
	s_mov_b64 s[22:23], 0xc00
	s_mov_b32 s31, 0x40004000
	v_mov_b32_e32 v173, v172
	v_mov_b32_e32 v192, 0
	v_mov_b32_e32 v193, 0
	s_mov_b32 s33, 0
	v_add_u32_e32 v180, v180, v177
	v_add_u32_e32 v181, v181, v177
	v_add_u32_e32 v182, v182, v177
	v_add_u32_e32 v183, v183, v177
	v_add_u32_e32 v184, v184, v177
	v_add_u32_e32 v185, v185, v177
	v_add_u32_e32 v186, v186, v177
	v_add_u32_e32 v187, v187, v177
	v_add_u32_e32 v188, v188, v177
	v_add_u32_e32 v189, v189, v177
	v_add_u32_e32 v190, v190, v177
	v_add_u32_e32 v191, v191, v177
	v_mov_b32_e32 v166, v176
	v_lshlrev_b32_e32 v242, 12, v164
	v_lshl_add_u32 v242, v162, 2, v242
	v_lshlrev_b32_e32 v243, 11, v162
	v_lshl_add_u32 v243, v164, 4, v243
	v_readfirstlane_b32 s42, v176
	s_or_b32 s42, s42, 0x8000
	s_mov_b32 m0, s42
	s_lshl_b32 s36, s30, 15
	s_add_u32 s54, s6, s36
	s_addc_u32 s55, s7, 0
	s_mov_b64 s[40:41], s[54:55]
	s_mov_b32 s45, 0
	s_mov_b32 s58, 0x40000
	s_mov_b32 s46, 0x180000
	s_mov_b64 s[48:49], s[12:13]
	s_cmp_lg_u64 s[14:15], 0
	s_cselect_b32 s57, 1, 0
	s_cmp_lg_u64 s[0:1], 0
	s_cselect_b32 s59, 1, 0
	s_mov_b32 s47, 0
	s_mov_b32 s60, 0
	s_mov_b32 s44, 0
	s_add_u32 s52, s50, 8
	s_addc_u32 s53, s51, 0
	global_load_dwordx2 v[174:175], v243, s[52:53] nt
	s_add_u32 s52, s50, 0x200000
	s_addc_u32 s53, s51, 0
	s_waitcnt vmcnt(1)
	v_cvt_f32_f16_e32 v250, v170
	v_cvt_f32_f16_sdwa v251, v170 dst_sel:DWORD dst_unused:UNUSED_PAD src0_sel:WORD_1
	v_cvt_f32_f16_e32 v252, v171
	v_cvt_f32_f16_sdwa v253, v171 dst_sel:DWORD dst_unused:UNUSED_PAD src0_sel:WORD_1
	v_pk_add_f32 v[198:199], v[130:131], v[134:135]
	v_pk_add_f32 v[200:201], v[132:133], v[136:137]
	v_mov_b32_e32 v194, 0
	v_mov_b32_e32 v195, 0
	v_mov_b32_e32 v196, 0
	v_mov_b32_e32 v197, 0
	v_pk_add_f32 v[198:199], v[198:199], v[250:251]
	v_pk_add_f32 v[200:201], v[200:201], v[252:253]
	v_lshrrev_b32_e32 v249, 4, v176
	v_and_b32_e32 v248, 15, v249
	v_bfe_u32 v246, v249, 4, 2
	v_lshrrev_b32_e32 v247, 8, v249
	v_and_b32_e32 v245, 3, v247
	v_lshrrev_b32_e32 v244, 2, v247
	v_lshl_add_u32 v246, v244, 2, v246
	v_lshl_add_u32 v246, v245, 3, v246
	v_mul_u32_u24_e32 v244, 33, v248
	v_add_u32_e32 v244, v244, v246
	s_mov_b32 s36, 0x12000
	v_lshl_add_u32 v244, v244, 2, s36
	v_bfe_u32 v246, v249, 5, 1
	v_lshl_add_u32 v246, v247, 1, v246
	v_and_b32_e32 v245, 31, v249
	v_lshl_add_u32 v247, s30, 4, v246
	v_lshlrev_b32_e32 v247, 12, v247
	v_lshrrev_b32_e32 v248, 10, v165
	v_and_b32_e32 v248, 31, v248
	v_lshl_add_u32 v248, v248, 5, v245
	v_lshl_add_u32 v247, v248, 2, v247
	v_mul_u32_u24_e32 v246, 33, v246
	v_add_u32_e32 v246, v246, v245
	v_lshl_add_u32 v246, v246, 2, s36
	s_branch .Lrec_act
	s_nop 0
	s_nop 0
	s_nop 0
	s_nop 0

.Lrec_own_ok:
	s_barrier
	ds_read_b32 v245, v246
	ds_read_b128 v[194:197], v180
	ds_read_b128 v[198:201], v181
	ds_read_b128 v[202:205], v182
	ds_read_b128 v[206:209], v183
	ds_read_b128 v[210:213], v184
	ds_read_b128 v[214:217], v185
	s_cmp_eq_u32 s59, 0
	s_cbranch_scc1 .Lrec_tail1
.Lrec_tail0:
	s_waitcnt lgkmcnt(5)
	v_mfma_f32_16x16x32_f16 v[154:157], v[82:85], v[194:197], v[154:157]
	ds_read_b128 v[218:221], v186
	s_waitcnt lgkmcnt(5)
	v_mfma_f32_16x16x32_f16 v[154:157], v[86:89], v[198:201], v[154:157]
	ds_read_b128 v[222:225], v187
	global_load_dwordx2 v[174:175], v243, s[52:53] nt
	s_waitcnt lgkmcnt(5)
	v_mfma_f32_16x16x32_f16 v[154:157], v[90:93], v[202:205], v[154:157]
	ds_read_b128 v[226:229], v188
	global_store_dword v247, v245, s[48:49] nt
	s_waitcnt lgkmcnt(5)
	v_mfma_f32_16x16x32_f16 v[154:157], v[94:97], v[206:209], v[154:157]
	ds_read_b128 v[230:233], v189
	s_mov_b64 exec, s[2:3]
	s_cmp_lg_u32 s57, 0
	s_cbranch_scc1 .Lrec_poi_sc1_0
	buffer_store_dwordx2 v[172:173], v165, s[8:11], s46 offen
	s_branch .Lrec_poi_done_0

.Lrec_tail1:
	s_waitcnt lgkmcnt(5)
	v_mfma_f32_16x16x32_f16 v[158:161], v[18:21], v[194:197], v[158:161]
	ds_read_b128 v[218:221], v186
	s_waitcnt lgkmcnt(5)
	v_mfma_f32_16x16x32_f16 v[158:161], v[22:25], v[198:201], v[158:161]
	ds_read_b128 v[222:225], v187
	global_load_dwordx2 v[174:175], v243, s[52:53] nt
	s_waitcnt lgkmcnt(5)
	v_mfma_f32_16x16x32_f16 v[158:161], v[26:29], v[202:205], v[158:161]
	ds_read_b128 v[226:229], v188
	global_store_dword v247, v245, s[48:49] nt
	s_waitcnt lgkmcnt(5)
	v_mfma_f32_16x16x32_f16 v[158:161], v[30:33], v[206:209], v[158:161]
	ds_read_b128 v[230:233], v189
	s_mov_b64 exec, s[2:3]
	s_cmp_lg_u32 s57, 0
	s_cbranch_scc1 .Lrec_poi_sc1_1
	buffer_store_dwordx2 v[172:173], v165, s[8:11], s46 offen
	s_branch .Lrec_poi_done_1

.Lrec_hst_done:
	s_mov_b64 exec, -1
	ds_write_b32 v244, v193
	s_cmpk_eq_i32 s33, 0x100
	s_cbranch_scc1 .Lrec_done
	s_waitcnt vmcnt(0)
	s_branch .Lrec_step

	.amdhsa_kernel _Z8lstm_recPKDF16_S0_PKfPhPf
		.amdhsa_group_segment_fixed_size 75840
		.amdhsa_private_segment_fixed_size 0
		.amdhsa_kernarg_size 40
		.amdhsa_user_sgpr_count 2
		.amdhsa_user_sgpr_dispatch_ptr 0
		.amdhsa_user_sgpr_queue_ptr 0
		.amdhsa_user_sgpr_kernarg_segment_ptr 1
		.amdhsa_user_sgpr_dispatch_id 0
		.amdhsa_user_sgpr_kernarg_preload_length 0
		.amdhsa_user_sgpr_kernarg_preload_offset 0
		.amdhsa_user_sgpr_private_segment_size 0
		.amdhsa_uses_dynamic_stack 0
		.amdhsa_enable_private_segment 0
		.amdhsa_system_sgpr_workgroup_id_x 1
		.amdhsa_system_sgpr_workgroup_id_y 0
		.amdhsa_system_sgpr_workgroup_id_z 0
		.amdhsa_system_sgpr_workgroup_info 0
		.amdhsa_system_vgpr_workitem_id 0
		.amdhsa_next_free_vgpr 256
		.amdhsa_next_free_sgpr 96
		.amdhsa_accum_offset 256
		.amdhsa_reserve_vcc 1
		.amdhsa_float_round_mode_32 0
		.amdhsa_float_round_mode_16_64 0
		.amdhsa_float_denorm_mode_32 3
		.amdhsa_float_denorm_mode_16_64 3
		.amdhsa_dx10_clamp 1
		.amdhsa_ieee_mode 1
		.amdhsa_fp16_overflow 0
		.amdhsa_tg_split 0
		.amdhsa_exception_fp_ieee_invalid_op 0
		.amdhsa_exception_fp_denorm_src 0
		.amdhsa_exception_fp_ieee_div_zero 0
		.amdhsa_exception_fp_ieee_overflow 0
		.amdhsa_exception_fp_ieee_underflow 0
		.amdhsa_exception_fp_ieee_inexact 0
		.amdhsa_exception_int_div_zero 0
	.end_amdhsa_kernel

amdhsa.kernels:
  - .agpr_count:     0
    .args:
      - .actual_access:  read_only
        .address_space:  global
        .offset:         0
        .size:           8
        .value_kind:     global_buffer
      - .actual_access:  write_only
        .address_space:  global
        .offset:         8
        .size:           8
        .value_kind:     global_buffer
      - .actual_access:  read_only
        .address_space:  global
        .offset:         16
        .size:           8
        .value_kind:     global_buffer
      - .actual_access:  read_only
        .address_space:  global
        .offset:         24
        .size:           8
        .value_kind:     global_buffer
      - .actual_access:  read_only
        .address_space:  global
        .offset:         32
        .size:           8
        .value_kind:     global_buffer
      - .actual_access:  read_only
        .address_space:  global
        .offset:         40
        .size:           8
        .value_kind:     global_buffer
      - .actual_access:  read_only
        .address_space:  global
        .offset:         48
        .size:           8
        .value_kind:     global_buffer
      - .actual_access:  read_only
        .address_space:  global
        .offset:         56
        .size:           8
        .value_kind:     global_buffer
      - .actual_access:  read_only
        .address_space:  global
        .offset:         64
        .size:           8
        .value_kind:     global_buffer
      - .actual_access:  read_only
        .address_space:  global
        .offset:         72
        .size:           8
        .value_kind:     global_buffer
      - .actual_access:  write_only
        .address_space:  global
        .offset:         80
        .size:           8
        .value_kind:     global_buffer
      - .actual_access:  write_only
        .address_space:  global
        .offset:         88
        .size:           8
        .value_kind:     global_buffer
      - .actual_access:  write_only
        .address_space:  global
        .offset:         96
        .size:           8
        .value_kind:     global_buffer
      - .actual_access:  write_only
        .address_space:  global
        .offset:         104
        .size:           8
        .value_kind:     global_buffer
    .group_segment_fixed_size: 0
    .kernarg_segment_align: 8
    .kernarg_segment_size: 112
    .language:       OpenCL C
    .language_version:
      - 2
      - 0
    .max_flat_workgroup_size: 256
    .name:           _Z4prepPKfPDF16_S0_S0_S0_S0_S0_S0_S0_S0_S1_S1_PfPh
    .private_segment_fixed_size: 0
    .sgpr_count:     32
    .sgpr_spill_count: 0
    .symbol:         _Z4prepPKfPDF16_S0_S0_S0_S0_S0_S0_S0_S0_S1_S1_PfPh.kd
    .uniform_work_group_size: 1
    .uses_dynamic_stack: false
    .vgpr_count:     16
    .vgpr_spill_count: 0
    .wavefront_size: 64
  - .agpr_count:     0
    .args:
      - .address_space:  global
        .offset:         0
        .size:           8
        .value_kind:     global_buffer
      - .address_space:  global
        .offset:         8
        .size:           8
        .value_kind:     global_buffer
      - .actual_access:  write_only
        .address_space:  global
        .offset:         16
        .size:           8
        .value_kind:     global_buffer
    .group_segment_fixed_size: 0
    .kernarg_segment_align: 8
    .kernarg_segment_size: 24
    .language:       OpenCL C
    .language_version:
      - 2
      - 0
    .max_flat_workgroup_size: 512
    .name:           _Z7gemm_zxPKDF16_S0_PDF16_
    .private_segment_fixed_size: 0
    .sgpr_count:     48
    .sgpr_spill_count: 0
    .symbol:         _Z7gemm_zxPKDF16_S0_PDF16_.kd
    .uniform_work_group_size: 1
    .uses_dynamic_stack: false
    .vgpr_count:     256
    .vgpr_spill_count: 0
    .wavefront_size: 64
  - .agpr_count:     0
    .args:
      - .actual_access:  read_only
        .address_space:  global
        .offset:         0
        .size:           8
        .value_kind:     global_buffer
      - .actual_access:  read_only
        .address_space:  global
        .offset:         8
        .size:           8
        .value_kind:     global_buffer
      - .actual_access:  read_only
        .address_space:  global
        .offset:         16
        .size:           8
        .value_kind:     global_buffer
      - .address_space:  global
        .offset:         24
        .size:           8
        .value_kind:     global_buffer
      - .actual_access:  write_only
        .address_space:  global
        .offset:         32
        .size:           8
        .value_kind:     global_buffer
    .group_segment_fixed_size: 75840
    .kernarg_segment_align: 8
    .kernarg_segment_size: 40
    .language:       OpenCL C
    .language_version:
      - 2
      - 0
    .max_flat_workgroup_size: 512
    .name:           _Z8lstm_recPKDF16_S0_PKfPhPf
    .private_segment_fixed_size: 0
    .sgpr_count:     80
    .sgpr_spill_count: 0
    .symbol:         _Z8lstm_recPKDF16_S0_PKfPhPf.kd
    .uniform_work_group_size: 1
    .uses_dynamic_stack: false
    .vgpr_count:     256
    .vgpr_spill_count: 0
    .wavefront_size: 64
